# phase 2 forget-gate cumsum: the 32 (b,h) sequences run on wave 0 of 32 different workgroups instead of all 8 waves of 4 workgroups (work distribution only, same math)
# speedup vs baseline: 1.0134x; 1.0134x over previous
; #define SB() __builtin_amdgcn_sched_barrier(0)
; __device__ __forceinline__ void post_elementwise(Frame& F, int l, const bool only_idem = false) {
;     ...
;     for (int bh = F.gw; bh < NB * 8; bh += F.NGW) { const int b = bh >> 3, h = bh & 7; const float* fl = WSP(float, WS_FLOG) + ((size_t)b * S + F.lane * 32) * 8 + h;
;         float v[32]; float s = 0.f;
; #pragma unroll
;         for (int i = 0; i < 32; ++i) v[i] = fl[i * 8];
;         SB();
; #pragma unroll
;         for (int i = 0; i < 32; ++i) { s += v[i]; v[i] = s; }
;         float incl = s;
; #pragma unroll
;         for (int o = 1; o < 64; o <<= 1) { const float n = __builtin_bit_cast(float, __builtin_amdgcn_ds_bpermute((F.lane - o) << 2, __builtin_bit_cast(int, incl))); if (F.lane >= o) incl += n; }
;         const float excl = incl - s; float* cb = WSP(float, WS_CB) + (size_t)bh * S + F.lane * 32;
.LBB0_642:
	s_mov_b32 s100, s38
	s_andn2_b32 s38, s38, 7
	s_cmp_eq_u32 s38, s100
	s_cselect_b32 s38, s38, 0x8000
	s_lshr_b32 s38, s38, 3
	v_readlane_b32 s70, v249, 46
	s_cmp_gt_i32 s38, 31
	v_readlane_b32 s66, v249, 35
	v_readlane_b32 s67, v249, 37
	v_readlane_b32 s71, v249, 47
	s_movk_i32 s76, 0x6000
	s_mov_b32 s77, 0xa000
	s_movk_i32 s80, 0x7000
	s_mov_b32 s10, 0xc13504f3
	s_cbranch_scc1 .LBB0_645
	v_lshlrev_b32_e32 v4, 5, v46
	v_ashrrev_i32_e32 v5, 31, v4
	s_waitcnt lgkmcnt(0)
	v_lshlrev_b64 v[2:3], 5, v[4:5]
	s_and_b32 s6, s38, 7
	v_lshl_add_u64 v[2:3], s[36:37], 0, v[2:3]
	s_lshl_b32 s34, s6, 2
	v_lshl_add_u64 v[2:3], v[2:3], 0, s[34:35]
	s_mov_b64 s[6:7], 0x2adc1000
	s_ashr_i32 s39, s38, 31
	v_lshl_add_u64 v[2:3], v[2:3], 0, s[6:7]
	s_lshl_b64 s[6:7], s[38:39], 13
	v_readlane_b32 s8, v249, 31
	s_add_u32 s8, s8, s4
	v_readlane_b32 s9, v249, 32
	s_addc_u32 s9, s9, s5
	s_add_u32 s6, s8, s6
	v_lshlrev_b32_e32 v10, 2, v46
	s_addc_u32 s7, s9, s7
	v_add_u32_e32 v0, -4, v10
	v_cmp_gt_i32_e32 vcc, 1, v46
	v_add_u32_e32 v6, -8, v10
	v_cmp_gt_i32_e64 s[56:57], 2, v46
	v_add_u32_e32 v7, -16, v10
	v_cmp_gt_i32_e64 s[58:59], 4, v46
	v_subrev_u32_e32 v8, 32, v10
	v_cmp_gt_i32_e64 s[60:61], 8, v46
	v_subrev_u32_e32 v9, 64, v10
	v_cmp_gt_i32_e64 s[62:63], 16, v46
	v_add_u32_e32 v10, 0xffffff80, v10
	v_cmp_gt_i32_e64 s[64:65], 32, v46
	v_lshl_add_u64 v[4:5], v[4:5], 2, s[6:7]
	s_mov_b32 s6, s38

; #define GAS __attribute__((address_space(1)))
; __device__ __forceinline__ void post_elementwise(Frame& F, int l, const bool only_idem = false) {
;     ...
;     if (!only_idem) { const float* kn = F.in[18] + l * 512; const float* qn = F.in[17] + l * 512; bf16_t* kc = WSP(bf16_t, WS_KC) + (size_t)l * TM * D;
;       f32x4 gg0 = *(const GAS f32x4*)(kn + F.lane * 8), gg1 = *(const GAS f32x4*)(kn + F.lane * 8 + 4); { const f32x4 q0 = *(const GAS f32x4*)(qn + F.lane * 8), q1 = *(const GAS f32x4*)(qn + F.lane * 8 + 4); gg0 = gg0 * q0; gg1 = gg1 * q1; }
;       for (int it = F.gw; it < TM * 4; it += F.NGW) { bf16_t* p = kc + (size_t)(it >> 2) * D + (it & 3) * 512 + F.lane * 8;
.LBB0_645:
	s_mov_b32 s38, s100
	s_cmpk_gt_i32 s38, 0xfff
	s_cbranch_scc1 .LBB0_648
	v_readlane_b32 s6, v248, 30
	s_mov_b32 s12, s6
	s_lshl_b32 s6, s6, 22
	v_readlane_b32 s7, v248, 31
	s_add_u32 s6, s36, s6
	s_load_dwordx4 s[8:11], s[40:41], 0x88
	s_addc_u32 s7, s37, 0
	s_add_u32 s6, s6, 0x336a1000
	s_addc_u32 s7, s7, 0
	s_lshl_b32 s34, s12, 9
	s_lshl_b64 s[12:13], s[34:35], 2
	s_waitcnt lgkmcnt(0)
	s_add_u32 s10, s10, s12
	s_addc_u32 s11, s11, s13
	s_add_u32 s8, s8, s12
	v_lshlrev_b64 v[2:3], 2, v[30:31]
	s_addc_u32 s9, s9, s13
	v_lshl_add_u64 v[12:13], s[10:11], 0, v[2:3]
	v_lshl_add_u64 v[2:3], s[8:9], 0, v[2:3]
	global_load_dwordx4 v[4:7], v[2:3], off offset:16
	global_load_dwordx4 v[8:11], v[12:13], off offset:16
	s_nop 0
	global_load_dwordx4 v[12:15], v[12:13], off
	s_nop 0
	global_load_dwordx4 v[16:19], v[2:3], off
	s_lshl_b32 s8, s38, 9
	v_readlane_b32 s12, v249, 33
	s_mov_b32 s13, 0x3d8293ee
	s_waitcnt vmcnt(2)
	v_pk_mul_f32 v[2:3], v[10:11], v[6:7]
	v_pk_mul_f32 v[4:5], v[8:9], v[4:5]
	s_waitcnt vmcnt(0)
	v_pk_mul_f32 v[6:7], v[14:15], v[18:19]
	v_pk_mul_f32 v[8:9], v[12:13], v[16:17]
